# QKV K-loop: no VALU at the head of the load segments (ds_read bases precomputed once per phase, LDS-DMA address adds moved behind the ds_read groups)
# baseline (speedup 1.0000x reference)
; #define PG8_STAGEA(bufoff, gbase, h) do { if constexpr (GATHER) { PG8_STAGE(bufoff, gbase, vA[h]); } else { PG8_STAGE(bufoff, (gbase) + (h) * hstepA, voffA); } } while (0)
; #define PG8_WAIT_V(n) asm volatile("s_waitcnt vmcnt(" #n ")" ::: "memory")
; #define PG8_BAR __builtin_amdgcn_s_barrier()
; #define PG8_CALCA(u, vo) do { _Pragma("unroll") for (int _h = 0; _h < 2; ++_h) _Pragma("unroll") for (int _i = 0; _i < 2; ++_i) \
;         vo[_h][_i] = Sched::ABLK ? ((unsigned)S.arow(u, 0) * (unsigned)lda + voffA[_i] + (unsigned)_h * 8192u) : ((unsigned)S.arow(u, _h * HALF + Rr[_i]) * (unsigned)lda + C2[_i]); } while (0)
; template <class Epi, class Sched>
; __device__ __forceinline__ void gemm_phase(const int tid, LAS unsigned char* lds, const char* Abase, const int lda, const int ldb, const int K, const Sched& S, const Epi& E) {
;     ...
;     for (int i = 0; i < 2; ++i) { int R, C; stage_rc(tid * 16 + i * 8192, R, C); const int Rb = Epi::WIDE ? ((R >> 5) * 64 + perm32(R & 31)) : ((R & ~31) + perm32(R & 31)); Rr[i] = R; C2[i] = (unsigned)C * 2u; voffB[i] = (unsigned)(Rb * ldb) + (unsigned)C * 2u;
;         voffA[i] = Sched::ABLK ? (unsigned)((C >> 5) * 16384 + R * 64 + (C & 31) * 2) : ((unsigned)(R * lda) + (unsigned)C * 2u); }
;     const size_t kstep = (size_t)(BK * 2);
;     const size_t hstepB = (size_t)(Epi::WIDE ? 32 : HALF) * ldb;
;     const size_t hstepA = GATHER ? (size_t)0 : (Sched::ABLK ? (size_t)8192 : (size_t)HALF * lda);
;     const size_t kstepA = Sched::ABLK ? (size_t)32768 : kstep;
;     const unsigned ldsw = (unsigned)wid * 1024u;
;     const int aoff = lds_byte(wr * 64 + fr, fq * 8), boff = lds_byte(wc * 32 + fr, fq * 8);
;     ...
;     if constexpr (GATHER) { PG8_CALCA(cur, vA); } else { cA = Abase + (size_t)S.arow(cur, 0) * lda + S.acolb(cur); }
;     const char* cB = cur.bptr;
;     PG8_STAGE(PG8_SB(0, 0), cB, voffB); PG8_STAGE(PG8_SB(0, 1), cB + hstepB, voffB); PG8_STAGEA(PG8_SA(0, 0), cA, 0); PG8_STAGEA(PG8_SA(0, 1), cA, 1);
;     if (wr == 1) PG8_BAR;
;     PG8_WAIT_V(2); PG8_BAR;
;     PG8_STAGE(PG8_SB(1, 0), cB + kstep, voffB); PG8_STAGEA(PG8_SA(1, 0), cA + kstepA, 0); PG8_STAGE(PG8_SB(1, 1), cB + hstepB + kstep, voffB);
;     PG8_WAIT_V(6); PG8_BAR;
.LBB0_199:
	s_add_u32 s42, s2, 0x43400000
	s_addc_u32 s43, s3, 0
	s_lshl_b32 s2, s51, 11
	s_add_i32 s2, s2, 0
	s_and_b32 s49, s51, 3
	s_add_i32 s48, s2, 0x24000
	s_lshl_b32 s44, s41, 13
	s_lshl_b32 s45, s49, 12
	s_add_u32 s2, s52, 0x80
	v_mov_b32_e32 v199, v3
	s_addc_u32 s3, s53, 0
	s_add_i32 m0, s9, 0x18000
	v_lshl_add_u64 v[4:5], s[2:3], 0, v[198:199]
	v_mov_b32_e32 v197, v3
	s_waitcnt vmcnt(2)
	s_barrier
	global_load_lds_dwordx4 v[4:5], off
	s_add_i32 m0, s9, 0x1a000
	v_lshl_add_u64 v[4:5], s[2:3], 0, v[196:197]
	s_add_u32 s2, s0, 0x80
	v_mov_b32_e32 v201, v3
	s_addc_u32 s3, s1, 0
	s_add_i32 s65, s9, 0x8000
	v_mov_b32_e32 v203, v3
	global_load_lds_dwordx4 v[4:5], off
	v_lshl_add_u64 v[4:5], s[2:3], 0, v[200:201]
	s_mov_b32 m0, s65
	s_add_i32 s66, s9, 0xa000
	global_load_lds_dwordx4 v[4:5], off
	v_lshl_add_u64 v[4:5], s[2:3], 0, v[202:203]
	s_add_u32 s2, s52, 0x8080
	s_mov_b32 m0, s66
	s_addc_u32 s3, s53, 0
	global_load_lds_dwordx4 v[4:5], off
	s_add_i32 m0, s9, 0x1c000
	v_lshl_add_u64 v[4:5], s[2:3], 0, v[198:199]
	global_load_lds_dwordx4 v[4:5], off
	v_lshl_add_u64 v[4:5], s[2:3], 0, v[196:197]
	s_add_i32 m0, s9, 0x1e000
	v_lshlrev_b32_e32 v6, 6, v251
	global_load_lds_dwordx4 v[4:5], off
	v_bfe_u32 v5, v251, 4, 2
	v_and_b32_e32 v6, 0x3c0, v6
	v_lshlrev_b32_e32 v8, 2, v251
	v_lshrrev_b32_e32 v4, 4, v251
	v_lshl_or_b32 v7, v5, 4, v6
	v_and_b32_e32 v8, 32, v8
	v_and_b32_e32 v10, 3, v251
	v_and_b32_e32 v11, 7, v251
	v_bitop3_b32 v9, v7, s44, v8 bitop3:0xde
	v_bitop3_b32 v201, v7, s45, v8 bitop3:0xde
	v_add_u32_e32 v230, 0x10000, v201
	v_add_u32_e32 v231, 0x14000, v201
	v_add_u32_e32 v234, 0x18000, v201
	v_add_u32_e32 v235, 0x1c000, v201
	s_cmp_gt_i32 s5, 0
	v_lshrrev_b32_e32 v7, 2, v251
	v_bitop3_b32 v4, v4, v11, 3 bitop3:0x6c
	v_bitop3_b32 v5, v5, v11, 4 bitop3:0x36
	v_lshlrev_b32_e32 v11, 1, v10
	v_bfe_u32 v12, v251, 2, 3
	s_waitcnt vmcnt(6)
	s_cselect_b64 s[44:45], -1, 0
	s_add_i32 s68, s5, -2
	v_bfe_u32 v8, v251, 2, 4
	v_bitop3_b32 v7, v7, v11, 7 bitop3:0x6c
	v_bitop3_b32 v11, v11, v12, 1 bitop3:0x36
	s_cmpk_lt_u32 s40, 0x100
	v_lshlrev_b32_e32 v4, 3, v4
	v_lshlrev_b32_e32 v5, 3, v5
	v_lshlrev_b32_e32 v7, 3, v7
	v_lshlrev_b32_e32 v11, 3, v11
	v_lshl_or_b32 v203, s41, 6, v8
	v_add_u32_e32 v6, s48, v6
	v_lshl_add_u32 v8, v8, 6, s48
	s_mov_b32 s85, s51
	s_mov_b32 s67, 0
	s_cselect_b64 s[46:47], -1, 0
	s_lshl_b32 s69, s49, 6
	v_lshlrev_b32_e32 v206, 4, v10
	v_mov_b32_e32 v207, v3
	v_add_u32_e32 v241, v6, v4
	v_add_u32_e32 v242, v6, v5
	v_add_u32_e32 v243, v8, v7
	v_add_u32_e32 v244, v8, v11
	v_add_u32_e32 v245, 0, v9
	v_readlane_b32 s73, v254, 4
	v_readlane_b32 s76, v254, 13
	s_barrier
	s_branch .LBB0_202

; #define PG8_STAGEA(bufoff, gbase, h) do { if constexpr (GATHER) { PG8_STAGE(bufoff, gbase, vA[h]); } else { PG8_STAGE(bufoff, (gbase) + (h) * hstepA, voffA); } } while (0)
; #define PG8_LDA(dst, b, h) do { _Pragma("unroll") for (int m = 0; m < 4; ++m) _Pragma("unroll") for (int k = 0; k < 2; ++k) dst[m][k] = *(const LAS bf16x8*)(lds + PG8_SA(b, h) + aoff + m * 2048 + k * 1024); } while (0)
; #define PG8_MM(ai, bj, At, Bt) do { if constexpr (Epi::F8MMA) PG8_MMA8(ai, bj, At, Bt##8); else PG8_MMA(ai, bj, At, Bt); } while (0)
; #define PG8_WAIT_V(n) asm volatile("s_waitcnt vmcnt(" #n ")" ::: "memory")
; #define PG8_WAIT_L(n) asm volatile("s_waitcnt lgkmcnt(" #n ")" ::: "memory")
; #define PG8_BAR __builtin_amdgcn_s_barrier()
; #define PG8_SCHED __builtin_amdgcn_sched_barrier(0)
; template <class Epi, class Sched>
; __device__ __forceinline__ void gemm_phase(const int tid, LAS unsigned char* lds, const char* Abase, const int lda, const int ldb, const int K, const Sched& S, const Epi& E) {
;     ...
;             PG8_WAIT_V(8); PG8_WAIT_L(0); PG8_BAR; PG8_MM(0, 0, At, B0); PG8_MM(0, 1, At, B1); PG8_BAR; PG8_SCHED;
;             PG8_LDA(At, 0, 1); PG8_STAGE(PG8_SB(0, 0), b2, voffB); PG8_STAGE(PG8_SB(0, 1), b2 + hstepB, voffB); PG8_STAGEA(PG8_SA(0, 0), a2, 0);
;             PG8_WAIT_V(8); PG8_WAIT_L(0); PG8_BAR; PG8_MM(1, 0, At, B0); PG8_MM(1, 1, At, B1); PG8_BAR; PG8_SCHED;
.LBB0_209:
	s_add_i32 s78, s78, 2
	s_and_b64 s[54:55], s[56:57], exec
	s_cselect_b32 s55, 0, s2
	s_cselect_b32 s54, 0, s3
	s_add_u32 s62, s0, s55
	s_addc_u32 s63, s1, s54
	s_add_u32 s60, s52, s2
	s_addc_u32 s61, s53, s3
	s_add_u32 s54, s62, 0x80
	s_addc_u32 s55, s63, 0
	s_waitcnt vmcnt(8)
	s_and_b64 s[56:57], s[56:57], exec
	s_waitcnt lgkmcnt(0)
	s_cselect_b32 s56, s50, s60
	s_cselect_b32 s57, s51, s61
	s_add_u32 s60, s56, 0x80
	s_addc_u32 s61, s57, 0
	s_barrier
	s_setprio 1
	v_mov_b32_e32 v205, s77
	s_waitcnt lgkmcnt(0)
	s_nop 0
	v_mfma_scale_f32_16x16x128_f8f6f4 v[192:195], v[20:27], v[60:67], v[192:195], v205, v216 op_sel_hi:[0,0,0]
	v_mfma_scale_f32_16x16x128_f8f6f4 v[188:191], v[28:35], v[60:67], v[188:191], v205, v216 op_sel_hi:[0,0,0]
	v_mfma_scale_f32_16x16x128_f8f6f4 v[176:179], v[20:27], v[52:59], v[176:179], v205, v216 op_sel_hi:[0,0,0]
	v_mfma_scale_f32_16x16x128_f8f6f4 v[172:175], v[28:35], v[52:59], v[172:175], v205, v216 op_sel_hi:[0,0,0]
	v_mfma_scale_f32_16x16x128_f8f6f4 v[160:163], v[20:27], v[44:51], v[160:163], v205, v216 op_sel_hi:[0,0,0]
	v_mfma_scale_f32_16x16x128_f8f6f4 v[156:159], v[28:35], v[44:51], v[156:159], v205, v216 op_sel_hi:[0,0,0]
	v_mfma_scale_f32_16x16x128_f8f6f4 v[144:147], v[20:27], v[36:43], v[144:147], v205, v216 op_sel_hi:[0,0,0]
	v_mfma_scale_f32_16x16x128_f8f6f4 v[140:143], v[28:35], v[36:43], v[140:143], v205, v216 op_sel_hi:[0,0,0]
	s_setprio 0
	s_setprio 1
	v_mfma_scale_f32_16x16x128_f8f6f4 v[184:187], v[4:11], v[60:67], v[184:187], v205, v216 op_sel_hi:[0,0,0]
	v_mfma_scale_f32_16x16x128_f8f6f4 v[180:183], v[12:19], v[60:67], v[180:183], v205, v216 op_sel_hi:[0,0,0]
	v_mfma_scale_f32_16x16x128_f8f6f4 v[168:171], v[4:11], v[52:59], v[168:171], v205, v216 op_sel_hi:[0,0,0]
	v_mfma_scale_f32_16x16x128_f8f6f4 v[164:167], v[12:19], v[52:59], v[164:167], v205, v216 op_sel_hi:[0,0,0]
	v_mfma_scale_f32_16x16x128_f8f6f4 v[152:155], v[4:11], v[44:51], v[152:155], v205, v216 op_sel_hi:[0,0,0]
	v_mfma_scale_f32_16x16x128_f8f6f4 v[148:151], v[12:19], v[44:51], v[148:151], v205, v216 op_sel_hi:[0,0,0]
	v_mfma_scale_f32_16x16x128_f8f6f4 v[136:139], v[4:11], v[36:43], v[136:139], v205, v216 op_sel_hi:[0,0,0]
	v_mfma_scale_f32_16x16x128_f8f6f4 v[132:135], v[12:19], v[36:43], v[132:135], v205, v216 op_sel_hi:[0,0,0]
	s_setprio 0
	s_barrier
	s_mov_b32 m0, s10
	s_add_u32 s82, s56, 0x8000
	ds_read_b128 v[36:39], v245 offset:16384
	ds_read_b128 v[40:43], v245 offset:17408
	ds_read_b128 v[44:47], v245 offset:18432
	ds_read_b128 v[48:51], v245 offset:19456
	ds_read_b128 v[52:55], v245 offset:20480
	ds_read_b128 v[56:59], v245 offset:21504
	ds_read_b128 v[60:63], v245 offset:22528
	ds_read_b128 v[64:67], v245 offset:23552
	v_lshl_add_u64 v[228:229], s[56:57], 0, v[198:199]
	global_load_lds_dwordx4 v[228:229], off
	v_lshl_add_u64 v[228:229], s[56:57], 0, v[196:197]
	s_mov_b32 m0, s11
	s_addc_u32 s83, s57, 0
	global_load_lds_dwordx4 v[228:229], off
	v_lshl_add_u64 v[228:229], s[82:83], 0, v[198:199]
	s_mov_b32 m0, s22
	s_nop 0
	global_load_lds_dwordx4 v[228:229], off
	v_lshl_add_u64 v[228:229], s[82:83], 0, v[196:197]
	s_mov_b32 m0, s25
	s_nop 0
	global_load_lds_dwordx4 v[228:229], off
	s_mov_b32 m0, s9
	s_nop 0
	global_load_lds_dwordx4 v200, s[62:63]
	s_mov_b32 m0, s28
	s_nop 0
	global_load_lds_dwordx4 v202, s[62:63]
	s_waitcnt vmcnt(8)
	s_waitcnt lgkmcnt(0)
	s_barrier
	s_setprio 1
	s_waitcnt lgkmcnt(0)
	v_mfma_scale_f32_16x16x128_f8f6f4 v[128:131], v[20:27], v[36:43], v[128:131], v205, v216 op_sel_hi:[0,0,0]
	v_mfma_scale_f32_16x16x128_f8f6f4 v[124:127], v[28:35], v[36:43], v[124:127], v205, v216 op_sel_hi:[0,0,0]
	v_mfma_scale_f32_16x16x128_f8f6f4 v[112:115], v[20:27], v[44:51], v[112:115], v205, v216 op_sel_hi:[0,0,0]
	v_mfma_scale_f32_16x16x128_f8f6f4 v[108:111], v[28:35], v[44:51], v[108:111], v205, v216 op_sel_hi:[0,0,0]
	v_mfma_scale_f32_16x16x128_f8f6f4 v[96:99], v[20:27], v[52:59], v[96:99], v205, v216 op_sel_hi:[0,0,0]
	v_mfma_scale_f32_16x16x128_f8f6f4 v[92:95], v[28:35], v[52:59], v[92:95], v205, v216 op_sel_hi:[0,0,0]
	v_mfma_scale_f32_16x16x128_f8f6f4 v[80:83], v[20:27], v[60:67], v[80:83], v205, v216 op_sel_hi:[0,0,0]
	v_mfma_scale_f32_16x16x128_f8f6f4 v[76:79], v[28:35], v[60:67], v[76:79], v205, v216 op_sel_hi:[0,0,0]
	s_setprio 0
	s_setprio 1
	v_mfma_scale_f32_16x16x128_f8f6f4 v[120:123], v[4:11], v[36:43], v[120:123], v205, v216 op_sel_hi:[0,0,0]
	v_mfma_scale_f32_16x16x128_f8f6f4 v[116:119], v[12:19], v[36:43], v[116:119], v205, v216 op_sel_hi:[0,0,0]
	v_mfma_scale_f32_16x16x128_f8f6f4 v[104:107], v[4:11], v[44:51], v[104:107], v205, v216 op_sel_hi:[0,0,0]
	v_mfma_scale_f32_16x16x128_f8f6f4 v[100:103], v[12:19], v[44:51], v[100:103], v205, v216 op_sel_hi:[0,0,0]
	v_mfma_scale_f32_16x16x128_f8f6f4 v[88:91], v[4:11], v[52:59], v[88:91], v205, v216 op_sel_hi:[0,0,0]
	v_mfma_scale_f32_16x16x128_f8f6f4 v[84:87], v[12:19], v[52:59], v[84:87], v205, v216 op_sel_hi:[0,0,0]
	v_mfma_scale_f32_16x16x128_f8f6f4 v[72:75], v[4:11], v[60:67], v[72:75], v205, v216 op_sel_hi:[0,0,0]
	v_mfma_scale_f32_16x16x128_f8f6f4 v[68:71], v[12:19], v[60:67], v[68:71], v205, v216 op_sel_hi:[0,0,0]
	s_setprio 0
	s_barrier
; #define PG8_STAGEA(bufoff, gbase, h) do { if constexpr (GATHER) { PG8_STAGE(bufoff, gbase, vA[h]); } else { PG8_STAGE(bufoff, (gbase) + (h) * hstepA, voffA); } } while (0)
; #define PG8_LDA(dst, b, h) do { _Pragma("unroll") for (int m = 0; m < 4; ++m) _Pragma("unroll") for (int k = 0; k < 2; ++k) dst[m][k] = *(const LAS bf16x8*)(lds + PG8_SA(b, h) + aoff + m * 2048 + k * 1024); } while (0)
; #define PG8_MM(ai, bj, At, Bt) do { if constexpr (Epi::F8MMA) PG8_MMA8(ai, bj, At, Bt##8); else PG8_MMA(ai, bj, At, Bt); } while (0)
; #define PG8_WAIT_V(n) asm volatile("s_waitcnt vmcnt(" #n ")" ::: "memory")
; #define PG8_WAIT_L(n) asm volatile("s_waitcnt lgkmcnt(" #n ")" ::: "memory")
; #define PG8_BAR __builtin_amdgcn_s_barrier()
; #define PG8_SCHED __builtin_amdgcn_sched_barrier(0)
; template <class Epi, class Sched>
; __device__ __forceinline__ void gemm_phase(const int tid, LAS unsigned char* lds, const char* Abase, const int lda, const int ldb, const int K, const Sched& S, const Epi& E) {
;     ...
;             PG8_LDB(B0, 0, 0); PG8_LDB(B1, 0, 1); PG8_SCHED; PG8_LDA(At, 0, 0); PG8_STAGEA(PG8_SA(1, 1), a1, 1);
;     ...
;             PG8_LDA(At, 0, 1); PG8_STAGE(PG8_SB(0, 0), b2, voffB); PG8_STAGE(PG8_SB(0, 1), b2 + hstepB, voffB); PG8_STAGEA(PG8_SA(0, 0), a2, 0);
;             PG8_WAIT_V(8); PG8_WAIT_L(0); PG8_BAR; PG8_MM(1, 0, At, B0); PG8_MM(1, 1, At, B1); PG8_BAR; PG8_SCHED;
;             PG8_LDB(B0, 1, 0); PG8_LDB(B1, 1, 1); PG8_SCHED; PG8_LDA(At, 1, 0); PG8_STAGEA(PG8_SA(0, 1), a2, 1);
;             PG8_WAIT_V(8); PG8_WAIT_L(0); PG8_BAR; PG8_MM(0, 0, At, B0); PG8_MM(0, 1, At, B1); PG8_BAR; PG8_SCHED;
;             PG8_LDA(At, 1, 1); PG8_STAGE(PG8_SB(1, 0), b3, voffB); PG8_STAGE(PG8_SB(1, 1), b3 + hstepB, voffB); PG8_STAGEA(PG8_SA(1, 0), a3, 0);
;             PG8_WAIT_V(8); PG8_WAIT_L(0); PG8_BAR; PG8_MM(1, 0, At, B0); PG8_MM(1, 1, At, B1); PG8_BAR; PG8_SCHED;
.Lmid_qkv:
	s_add_i32 s79, 0, 0x18000
	s_add_i32 s82, 0, 0x1c000
	ds_read_b128 v[4:7], v234
	ds_read_b128 v[8:11], v234 offset:1024
	ds_read_b128 v[12:15], v234 offset:2048
	ds_read_b128 v[16:19], v234 offset:3072
	ds_read_b128 v[20:23], v235
	ds_read_b128 v[24:27], v235 offset:1024
	ds_read_b128 v[28:31], v235 offset:2048
	ds_read_b128 v[32:35], v235 offset:3072
	s_mov_b32 m0, s29
	ds_read_b128 v[36:39], v245 offset:32768
	ds_read_b128 v[40:43], v245 offset:33792
	ds_read_b128 v[44:47], v245 offset:34816
	ds_read_b128 v[48:51], v245 offset:35840
	ds_read_b128 v[52:55], v245 offset:36864
	ds_read_b128 v[56:59], v245 offset:37888
	ds_read_b128 v[60:63], v245 offset:38912
	ds_read_b128 v[64:67], v245 offset:39936
	v_lshl_add_u64 v[214:215], s[62:63], 0, v[214:215]
	global_load_lds_dwordx4 v[214:215], off
	v_lshl_add_u64 v[212:213], s[62:63], 0, v[212:213]
	s_mov_b32 m0, s64
	s_nop 0
	global_load_lds_dwordx4 v[212:213], off
	s_waitcnt vmcnt(8)
	s_waitcnt lgkmcnt(0)
	s_barrier
	s_setprio 1
	s_waitcnt lgkmcnt(0)
	v_mfma_scale_f32_16x16x128_f8f6f4 v[192:195], v[4:11], v[36:43], v[192:195], v205, v216 op_sel_hi:[0,0,0]
	v_mfma_scale_f32_16x16x128_f8f6f4 v[188:191], v[12:19], v[36:43], v[188:191], v205, v216 op_sel_hi:[0,0,0]
	v_mfma_scale_f32_16x16x128_f8f6f4 v[176:179], v[4:11], v[44:51], v[176:179], v205, v216 op_sel_hi:[0,0,0]
	v_mfma_scale_f32_16x16x128_f8f6f4 v[172:175], v[12:19], v[44:51], v[172:175], v205, v216 op_sel_hi:[0,0,0]
	v_mfma_scale_f32_16x16x128_f8f6f4 v[160:163], v[4:11], v[52:59], v[160:163], v205, v216 op_sel_hi:[0,0,0]
	v_mfma_scale_f32_16x16x128_f8f6f4 v[156:159], v[12:19], v[52:59], v[156:159], v205, v216 op_sel_hi:[0,0,0]
	v_mfma_scale_f32_16x16x128_f8f6f4 v[144:147], v[4:11], v[60:67], v[144:147], v205, v216 op_sel_hi:[0,0,0]
	v_mfma_scale_f32_16x16x128_f8f6f4 v[140:143], v[12:19], v[60:67], v[140:143], v205, v216 op_sel_hi:[0,0,0]
	s_setprio 0
	s_setprio 1
	v_mfma_scale_f32_16x16x128_f8f6f4 v[184:187], v[20:27], v[36:43], v[184:187], v205, v216 op_sel_hi:[0,0,0]
	v_mfma_scale_f32_16x16x128_f8f6f4 v[180:183], v[28:35], v[36:43], v[180:183], v205, v216 op_sel_hi:[0,0,0]
	v_mfma_scale_f32_16x16x128_f8f6f4 v[168:171], v[20:27], v[44:51], v[168:171], v205, v216 op_sel_hi:[0,0,0]
	v_mfma_scale_f32_16x16x128_f8f6f4 v[164:167], v[28:35], v[44:51], v[164:167], v205, v216 op_sel_hi:[0,0,0]
	v_mfma_scale_f32_16x16x128_f8f6f4 v[152:155], v[20:27], v[52:59], v[152:155], v205, v216 op_sel_hi:[0,0,0]
	v_mfma_scale_f32_16x16x128_f8f6f4 v[148:151], v[28:35], v[52:59], v[148:151], v205, v216 op_sel_hi:[0,0,0]
	v_mfma_scale_f32_16x16x128_f8f6f4 v[136:139], v[20:27], v[60:67], v[136:139], v205, v216 op_sel_hi:[0,0,0]
	v_mfma_scale_f32_16x16x128_f8f6f4 v[132:135], v[28:35], v[60:67], v[132:135], v205, v216 op_sel_hi:[0,0,0]
	s_setprio 0
	s_barrier
	s_add_i32 s62, s79, s8
	s_mov_b32 m0, s62
	ds_read_b128 v[36:39], v245 offset:49152
	ds_read_b128 v[40:43], v245 offset:50176
	ds_read_b128 v[44:47], v245 offset:51200
	ds_read_b128 v[48:51], v245 offset:52224
	ds_read_b128 v[52:55], v245 offset:53248
	ds_read_b128 v[56:59], v245 offset:54272
	ds_read_b128 v[60:63], v245 offset:55296
	ds_read_b128 v[64:67], v245 offset:56320
	v_lshl_add_u64 v[212:213], s[60:61], 0, v[198:199]
	global_load_lds_dwordx4 v[212:213], off
	s_add_i32 m0, s62, 0x2000
	s_add_u32 s56, s56, 0x8080
	v_lshl_add_u64 v[212:213], s[60:61], 0, v[196:197]
	s_addc_u32 s57, s57, 0
	s_add_i32 s60, s82, s8
	global_load_lds_dwordx4 v[212:213], off
	v_lshl_add_u64 v[212:213], s[56:57], 0, v[198:199]
	s_mov_b32 m0, s60
	s_nop 0
	global_load_lds_dwordx4 v[212:213], off
	v_lshl_add_u64 v[212:213], s[56:57], 0, v[196:197]
	s_add_i32 m0, s60, 0x2000
	s_nop 0
	global_load_lds_dwordx4 v[212:213], off
	s_mov_b32 m0, s65
	s_nop 0
	global_load_lds_dwordx4 v200, s[54:55]
	s_mov_b32 m0, s66
	s_nop 0
	global_load_lds_dwordx4 v202, s[54:55]
	s_waitcnt vmcnt(8)
	s_waitcnt lgkmcnt(0)
	s_barrier
	s_setprio 1
	s_waitcnt lgkmcnt(0)
	v_mfma_scale_f32_16x16x128_f8f6f4 v[128:131], v[4:11], v[36:43], v[128:131], v205, v216 op_sel_hi:[0,0,0]
	v_mfma_scale_f32_16x16x128_f8f6f4 v[124:127], v[12:19], v[36:43], v[124:127], v205, v216 op_sel_hi:[0,0,0]
	v_mfma_scale_f32_16x16x128_f8f6f4 v[112:115], v[4:11], v[44:51], v[112:115], v205, v216 op_sel_hi:[0,0,0]
	v_mfma_scale_f32_16x16x128_f8f6f4 v[108:111], v[12:19], v[44:51], v[108:111], v205, v216 op_sel_hi:[0,0,0]
	v_mfma_scale_f32_16x16x128_f8f6f4 v[96:99], v[4:11], v[52:59], v[96:99], v205, v216 op_sel_hi:[0,0,0]
	v_mfma_scale_f32_16x16x128_f8f6f4 v[92:95], v[12:19], v[52:59], v[92:95], v205, v216 op_sel_hi:[0,0,0]
	v_mfma_scale_f32_16x16x128_f8f6f4 v[80:83], v[4:11], v[60:67], v[80:83], v205, v216 op_sel_hi:[0,0,0]
	v_mfma_scale_f32_16x16x128_f8f6f4 v[76:79], v[12:19], v[60:67], v[76:79], v205, v216 op_sel_hi:[0,0,0]
	s_setprio 0
	s_setprio 1
	v_mfma_scale_f32_16x16x128_f8f6f4 v[120:123], v[20:27], v[36:43], v[120:123], v205, v216 op_sel_hi:[0,0,0]
	v_mfma_scale_f32_16x16x128_f8f6f4 v[116:119], v[28:35], v[36:43], v[116:119], v205, v216 op_sel_hi:[0,0,0]
	v_mfma_scale_f32_16x16x128_f8f6f4 v[104:107], v[20:27], v[44:51], v[104:107], v205, v216 op_sel_hi:[0,0,0]
	v_mfma_scale_f32_16x16x128_f8f6f4 v[100:103], v[28:35], v[44:51], v[100:103], v205, v216 op_sel_hi:[0,0,0]
	v_mfma_scale_f32_16x16x128_f8f6f4 v[88:91], v[20:27], v[52:59], v[88:91], v205, v216 op_sel_hi:[0,0,0]
	v_mfma_scale_f32_16x16x128_f8f6f4 v[84:87], v[28:35], v[52:59], v[84:87], v205, v216 op_sel_hi:[0,0,0]
	v_mfma_scale_f32_16x16x128_f8f6f4 v[72:75], v[20:27], v[60:67], v[72:75], v205, v216 op_sel_hi:[0,0,0]
	v_mfma_scale_f32_16x16x128_f8f6f4 v[68:71], v[28:35], v[60:67], v[68:71], v205, v216 op_sel_hi:[0,0,0]
	s_setprio 0
	s_barrier
	s_add_u32 s2, s2, 0x100
	s_addc_u32 s3, s3, 0
	s_cmp_ge_i32 s78, s5
	s_cbranch_scc1 .LBB0_212
.LBB0_210:
	ds_read_b128 v[20:23], v230
	ds_read_b128 v[24:27], v230 offset:1024
	ds_read_b128 v[28:31], v230 offset:2048
	ds_read_b128 v[32:35], v230 offset:3072
	ds_read_b128 v[4:7], v231
	ds_read_b128 v[8:11], v231 offset:1024
	ds_read_b128 v[12:15], v231 offset:2048
	ds_read_b128 v[16:19], v231 offset:3072
	s_cmp_eq_u32 s68, s78
	s_cselect_b64 s[56:57], -1, 0
	s_add_u32 s54, s0, s2
	s_addc_u32 s55, s1, s3
	s_add_u32 s54, s54, 0xffffff80
	s_addc_u32 s55, s55, -1
	s_add_i32 m0, s9, 0xc000
	s_add_i32 s60, s9, 0xe000
	s_cmp_lg_u32 s68, s78
	ds_read_b128 v[60:63], v245
	ds_read_b128 v[64:67], v245 offset:1024
	ds_read_b128 v[52:55], v245 offset:2048
	ds_read_b128 v[56:59], v245 offset:3072
	ds_read_b128 v[44:47], v245 offset:4096
	ds_read_b128 v[48:51], v245 offset:5120
	ds_read_b128 v[36:39], v245 offset:6144
	ds_read_b128 v[40:43], v245 offset:7168
	global_load_lds_dwordx4 v2, s[54:55]
	s_mov_b32 m0, s60
	s_nop 0
	global_load_lds_dwordx4 v204, s[54:55]
	s_cbranch_scc0 .LBB0_208
	v_mov_b32_e32 v205, v3
	v_mov_b64_e32 v[212:213], v[204:205]
	v_mov_b64_e32 v[214:215], v[2:3]
	s_cmp_eq_u32 s78, 0
	s_cbranch_scc1 .Lpeel_qkv
	s_branch .LBB0_209
